# scores: per-lane k-group permutation (g->y(g)) in the q'/key fragment reads to remove 2-way LDS bank conflicts of the 16-row ds_read_b128 pattern
# speedup vs baseline: 1.0121x; 1.0121x over previous
_Z7na_mainPKDF16_PKhS0_PKfS4_S4_S4_Pf:
	s_lshl_b32 s3, s2, 5
	s_and_b32 s3, s3, 0xe0
	s_ashr_i32 s2, s2, 3
	s_add_i32 s3, s3, s2
	s_ashr_i32 s2, s3, 6
	s_lshl_b32 s3, s3, 5
	s_and_b32 s14, s3, 0x7e0
	v_mov_b32_e32 v1, 0x7c0
	s_load_dwordx8 s[4:11], s[0:1], 0x0
	s_load_dwordx2 s[18:19], s[0:1], 0x20
	v_med3_u32 v1, s14, 32, v1
	v_subrev_u32_e32 v97, 32, v1
	s_ashr_i32 s3, s2, 31
	v_lshlrev_b32_e32 v58, 1, v97
	s_lshl_b64 s[12:13], s[2:3], 12
	v_mov_b32_e32 v59, 0
	v_sub_u32_e32 v60, s14, v97
	v_lshl_add_u64 v[10:11], s[12:13], 0, v[58:59]
	v_lshlrev_b64 v[2:3], 9, v[10:11]
	v_lshl_or_b32 v22, v60, 6, v0
	s_waitcnt lgkmcnt(0)
	v_and_b32_e32 v208, 31, v0
	v_lshlrev_b32_e32 v208, 5, v208
	global_load_dwordx4 v[192:195], v208, s[18:19]
	global_load_dwordx4 v[196:199], v208, s[18:19] offset:16
	v_lshl_add_u64 v[20:21], s[4:5], 0, v[2:3]
	v_ashrrev_i32_e32 v23, 31, v22
	v_lshl_add_u64 v[2:3], v[22:23], 4, v[20:21]
	global_load_dwordx4 v[12:15], v[2:3], off
	v_or_b32_e32 v28, 0x200, v22
	v_ashrrev_i32_e32 v29, 31, v28
	v_lshl_add_u64 v[2:3], v[28:29], 4, v[20:21]
	global_load_dwordx4 v[16:19], v[2:3], off
	v_or_b32_e32 v184, 0x400, v22
	v_ashrrev_i32_e32 v185, 31, v184
	v_lshl_add_u64 v[184:185], v[184:185], 4, v[20:21]
	v_or_b32_e32 v188, 0x600, v22
	v_ashrrev_i32_e32 v189, 31, v188
	v_lshl_add_u64 v[188:189], v[188:189], 4, v[20:21]
	global_load_dwordx4 v[184:187], v[184:185], off
	global_load_dwordx4 v[188:191], v[188:189], off
	v_lshrrev_b32_e32 v99, 6, v0
	v_and_b32_e32 v98, 63, v0
	v_lshlrev_b32_e32 v118, 13, v99
	v_lshl_or_b32 v58, v98, 5, v118
	s_movk_i32 s15, 0x1000
	v_lshl_add_u64 v[24:25], s[6:7], 0, v[58:59]
	v_or_b32_e32 v32, 0x400, v22
	v_or_b32_e32 v62, 0x600, v22
	v_add_co_u32_e32 v64, vcc, s15, v24
	s_mov_b64 s[12:13], 0x1000
	s_mov_b64 s[16:17], 0x1800
	v_lshlrev_b32_e32 v72, 1, v60
	v_lshrrev_b32_e32 v23, 5, v22
	v_and_b32_e32 v34, 32, v22
	v_ashrrev_i32_e32 v33, 31, v32
	v_ashrrev_i32_e32 v63, 31, v62
	v_addc_co_u32_e32 v65, vcc, 0, v25, vcc
	global_load_dwordx4 v[6:9], v58, s[6:7] offset:16
	global_load_dwordx4 v[2:5], v58, s[6:7]
	global_load_dwordx4 v[54:57], v58, s[6:7] offset:2064
	global_load_dwordx4 v[50:53], v58, s[6:7] offset:2048
	v_lshrrev_b32_e32 v58, 6, v22
	v_bfe_u32 v73, v22, 8, 2
	v_lshl_add_u64 v[26:27], v[24:25], 0, s[12:13]
	v_lshl_add_u64 v[24:25], v[24:25], 0, s[16:17]
	v_cmp_ne_u32_e32 vcc, 0, v34
	v_sub_u32_e32 v75, v23, v72
	global_load_dwordx4 v[42:45], v[64:65], off
	global_load_dwordx4 v[46:49], v[26:27], off offset:16
	global_load_dwordx4 v[34:37], v[64:65], off offset:2048
	global_load_dwordx4 v[38:41], v[24:25], off offset:16
	v_mov_b32_e32 v61, 0x60
	v_cndmask_b32_e32 v74, 0, v61, vcc
	v_add_u32_e32 v33, v74, v58
	v_lshlrev_b32_e32 v64, 2, v33
	v_bfe_u32 v96, v0, 4, 1
	v_and_b32_e32 v100, 15, v0
	v_mov_b32_e32 v30, v59
	v_mov_b32_e32 v31, v59
	v_and_b32_e32 v64, 12, v64
	v_mul_u32_u24_e32 v29, 0xc000, v96
	v_bitop3_b32 v64, v64, v100, v73 bitop3:0x36
	v_lshl_or_b32 v64, v64, 4, v29
	v_lshlrev_b32_e32 v63, 1, v75
	v_lshl_add_u32 v33, v33, 8, v64
	v_bfe_u32 v71, v0, 1, 4
	v_and_b32_e32 v70, 32, v0
	v_lshlrev_b32_e32 v1, 3, v0
	v_lshrrev_b32_e32 v58, 1, v75
	v_and_b32_e32 v1, 8, v1
	v_add_lshl_u32 v58, v58, v70, 8
	v_lshlrev_b32_e32 v121, 3, v99
	v_bfe_u32 v101, v0, 4, 2
	v_lshlrev_b32_e32 v102, 2, v101
	v_and_b32_e32 v116, 31, v0
	v_bfe_u32 v119, v0, 5, 1
	v_lshlrev_b32_e32 v124, 1, v119
	v_lshlrev_b32_e32 v117, 8, v116
	v_lshrrev_b32_e32 v95, 4, v0
	s_movk_i32 s16, 0x60
	s_mov_b32 s17, 0xc000
	v_and_b32_e32 v211, 3, v99
	v_lshrrev_b32_e32 v212, 2, v99
	v_lshl_or_b32 v211, v211, 2, v212
	v_xor_b32_e32 v213, v100, v211
	v_mul_u32_u24_e32 v214, 0x60, v119
	v_add3_u32 v214, v214, v60, v99
	v_mul_u32_u24_e32 v215, 0xc000, v96
	v_lshl_add_u32 v214, v214, 8, v215
	v_lshl_or_b32 v220, v213, 4, v214
	v_xor_b32_e32 v221, 32, v220
	v_xor_b32_e32 v216, v71, v211
	v_lshl_add_u32 v217, v119, 5, v99
	v_lshlrev_b32_e32 v217, 8, v217
	v_lshl_or_b32 v216, v216, 4, v217
	v_or_b32_e32 v216, v216, v1
	v_add_u32_e32 v222, 0x23800, v216
	v_xor_b32_e32 v223, 32, v222
	s_waitcnt vmcnt(11)
	ds_write_b128 v220, v[12:15]
	v_fma_mix_f32 v200, v192, v12, 0 op_sel_hi:[0,1,0]
	v_fma_mix_f32 v201, v193, v12, 0 op_sel:[0,1,0] op_sel_hi:[0,1,0]
	v_cvt_f32_f16_e32 v211, v12
	v_cvt_f32_f16_sdwa v212, v12 dst_sel:DWORD dst_unused:UNUSED_PAD src0_sel:WORD_1
	v_fma_mix_f32 v200, v194, v13, v200 op_sel_hi:[0,1,0]
	v_fma_mix_f32 v201, v195, v13, v201 op_sel:[0,1,0] op_sel_hi:[0,1,0]
	v_cvt_f32_f16_e32 v213, v13
	v_cvt_f32_f16_sdwa v214, v13 dst_sel:DWORD dst_unused:UNUSED_PAD src0_sel:WORD_1
	v_fma_mix_f32 v200, v196, v14, v200 op_sel_hi:[0,1,0]
	v_fma_mix_f32 v201, v197, v14, v201 op_sel:[0,1,0] op_sel_hi:[0,1,0]
	v_cvt_f32_f16_e32 v215, v14
	v_cvt_f32_f16_sdwa v216, v14 dst_sel:DWORD dst_unused:UNUSED_PAD src0_sel:WORD_1
	v_fma_mix_f32 v200, v198, v15, v200 op_sel_hi:[0,1,0]
	v_fma_mix_f32 v201, v199, v15, v201 op_sel:[0,1,0] op_sel_hi:[0,1,0]
	v_cvt_f32_f16_e32 v217, v15
	v_cvt_f32_f16_sdwa v218, v15 dst_sel:DWORD dst_unused:UNUSED_PAD src0_sel:WORD_1
	v_cvt_pk_fp8_f32 v224, v211, v212
	v_cvt_pk_fp8_f32 v225, v215, v216
	v_cvt_pk_fp8_f32 v224, v213, v214 op_sel:[0,0,1]
	v_cvt_pk_fp8_f32 v225, v217, v218 op_sel:[0,0,1]
	s_nop 0
	ds_write_b64 v222, v[224:225]
	s_waitcnt vmcnt(10)
	ds_write_b128 v221, v[16:19] offset:2048
	v_fma_mix_f32 v202, v192, v16, 0 op_sel_hi:[0,1,0]
	v_fma_mix_f32 v203, v193, v16, 0 op_sel:[0,1,0] op_sel_hi:[0,1,0]
	v_cvt_f32_f16_e32 v211, v16
	v_cvt_f32_f16_sdwa v212, v16 dst_sel:DWORD dst_unused:UNUSED_PAD src0_sel:WORD_1
	v_fma_mix_f32 v202, v194, v17, v202 op_sel_hi:[0,1,0]
	v_fma_mix_f32 v203, v195, v17, v203 op_sel:[0,1,0] op_sel_hi:[0,1,0]
	v_cvt_f32_f16_e32 v213, v17
	v_cvt_f32_f16_sdwa v214, v17 dst_sel:DWORD dst_unused:UNUSED_PAD src0_sel:WORD_1
	v_fma_mix_f32 v202, v196, v18, v202 op_sel_hi:[0,1,0]
	v_fma_mix_f32 v203, v197, v18, v203 op_sel:[0,1,0] op_sel_hi:[0,1,0]
	v_cvt_f32_f16_e32 v215, v18
	v_cvt_f32_f16_sdwa v216, v18 dst_sel:DWORD dst_unused:UNUSED_PAD src0_sel:WORD_1
	v_fma_mix_f32 v202, v198, v19, v202 op_sel_hi:[0,1,0]
	v_fma_mix_f32 v203, v199, v19, v203 op_sel:[0,1,0] op_sel_hi:[0,1,0]
	v_cvt_f32_f16_e32 v217, v19
	v_cvt_f32_f16_sdwa v218, v19 dst_sel:DWORD dst_unused:UNUSED_PAD src0_sel:WORD_1
	v_cvt_pk_fp8_f32 v226, v211, v212
	v_cvt_pk_fp8_f32 v227, v215, v216
	v_cvt_pk_fp8_f32 v226, v213, v214 op_sel:[0,0,1]
	v_cvt_pk_fp8_f32 v227, v217, v218 op_sel:[0,0,1]
	s_nop 0
	ds_write_b64 v223, v[226:227] offset:2048
	s_waitcnt vmcnt(9)
	ds_write_b128 v220, v[184:187] offset:4096
	v_fma_mix_f32 v204, v192, v184, 0 op_sel_hi:[0,1,0]
	v_fma_mix_f32 v205, v193, v184, 0 op_sel:[0,1,0] op_sel_hi:[0,1,0]
	v_cvt_f32_f16_e32 v211, v184
	v_cvt_f32_f16_sdwa v212, v184 dst_sel:DWORD dst_unused:UNUSED_PAD src0_sel:WORD_1
	v_fma_mix_f32 v204, v194, v185, v204 op_sel_hi:[0,1,0]
	v_fma_mix_f32 v205, v195, v185, v205 op_sel:[0,1,0] op_sel_hi:[0,1,0]
	v_cvt_f32_f16_e32 v213, v185
	v_cvt_f32_f16_sdwa v214, v185 dst_sel:DWORD dst_unused:UNUSED_PAD src0_sel:WORD_1
	v_fma_mix_f32 v204, v196, v186, v204 op_sel_hi:[0,1,0]
	v_fma_mix_f32 v205, v197, v186, v205 op_sel:[0,1,0] op_sel_hi:[0,1,0]
	v_cvt_f32_f16_e32 v215, v186
	v_cvt_f32_f16_sdwa v216, v186 dst_sel:DWORD dst_unused:UNUSED_PAD src0_sel:WORD_1
	v_fma_mix_f32 v204, v198, v187, v204 op_sel_hi:[0,1,0]
	v_fma_mix_f32 v205, v199, v187, v205 op_sel:[0,1,0] op_sel_hi:[0,1,0]
	v_cvt_f32_f16_e32 v217, v187
	v_cvt_f32_f16_sdwa v218, v187 dst_sel:DWORD dst_unused:UNUSED_PAD src0_sel:WORD_1
	v_cvt_pk_fp8_f32 v228, v211, v212
	v_cvt_pk_fp8_f32 v229, v215, v216
	v_cvt_pk_fp8_f32 v228, v213, v214 op_sel:[0,0,1]
	v_cvt_pk_fp8_f32 v229, v217, v218 op_sel:[0,0,1]
	s_nop 0
	ds_write_b64 v222, v[228:229] offset:4096
	s_waitcnt vmcnt(8)
	ds_write_b128 v221, v[188:191] offset:6144
	v_fma_mix_f32 v206, v192, v188, 0 op_sel_hi:[0,1,0]
	v_fma_mix_f32 v207, v193, v188, 0 op_sel:[0,1,0] op_sel_hi:[0,1,0]
	v_cvt_f32_f16_e32 v211, v188
	v_cvt_f32_f16_sdwa v212, v188 dst_sel:DWORD dst_unused:UNUSED_PAD src0_sel:WORD_1
	v_fma_mix_f32 v206, v194, v189, v206 op_sel_hi:[0,1,0]
	v_fma_mix_f32 v207, v195, v189, v207 op_sel:[0,1,0] op_sel_hi:[0,1,0]
	v_cvt_f32_f16_e32 v213, v189
	v_cvt_f32_f16_sdwa v214, v189 dst_sel:DWORD dst_unused:UNUSED_PAD src0_sel:WORD_1
	v_fma_mix_f32 v206, v196, v190, v206 op_sel_hi:[0,1,0]
	v_fma_mix_f32 v207, v197, v190, v207 op_sel:[0,1,0] op_sel_hi:[0,1,0]
	v_cvt_f32_f16_e32 v215, v190
	v_cvt_f32_f16_sdwa v216, v190 dst_sel:DWORD dst_unused:UNUSED_PAD src0_sel:WORD_1
	v_fma_mix_f32 v206, v198, v191, v206 op_sel_hi:[0,1,0]
	v_fma_mix_f32 v207, v199, v191, v207 op_sel:[0,1,0] op_sel_hi:[0,1,0]
	v_cvt_f32_f16_e32 v217, v191
	v_cvt_f32_f16_sdwa v218, v191 dst_sel:DWORD dst_unused:UNUSED_PAD src0_sel:WORD_1
	v_cvt_pk_fp8_f32 v230, v211, v212
	v_cvt_pk_fp8_f32 v231, v215, v216
	v_cvt_pk_fp8_f32 v230, v213, v214 op_sel:[0,0,1]
	v_cvt_pk_fp8_f32 v231, v217, v218 op_sel:[0,0,1]
	s_nop 0
	ds_write_b64 v223, v[230:231] offset:6144
	v_add_f32_e32 v200, v200, v201
	v_add_f32_e32 v202, v202, v203
	v_add_f32_e32 v204, v204, v205
	v_add_f32_e32 v206, v206, v207
	v_lshlrev_b32_e32 v208, 7, v119
	v_lshl_add_u32 v208, v99, 2, v208
	v_add_u32_e32 v208, 0x27800, v208
	v_add_f32_dpp v200, v200, v200 quad_perm:[1,0,3,2] row_mask:0xf bank_mask:0xf
	v_add_f32_dpp v202, v202, v202 quad_perm:[1,0,3,2] row_mask:0xf bank_mask:0xf
	v_add_f32_dpp v204, v204, v204 quad_perm:[1,0,3,2] row_mask:0xf bank_mask:0xf
	v_add_f32_dpp v206, v206, v206 quad_perm:[1,0,3,2] row_mask:0xf bank_mask:0xf
	v_add_f32_dpp v200, v200, v200 quad_perm:[2,3,0,1] row_mask:0xf bank_mask:0xf
	v_add_f32_dpp v202, v202, v202 quad_perm:[2,3,0,1] row_mask:0xf bank_mask:0xf
	v_add_f32_dpp v204, v204, v204 quad_perm:[2,3,0,1] row_mask:0xf bank_mask:0xf
	v_add_f32_dpp v206, v206, v206 quad_perm:[2,3,0,1] row_mask:0xf bank_mask:0xf
	v_add_f32_dpp v200, v200, v200 row_half_mirror row_mask:0xf bank_mask:0xf
	v_add_f32_dpp v202, v202, v202 row_half_mirror row_mask:0xf bank_mask:0xf
	v_add_f32_dpp v204, v204, v204 row_half_mirror row_mask:0xf bank_mask:0xf
	v_add_f32_dpp v206, v206, v206 row_half_mirror row_mask:0xf bank_mask:0xf
	v_add_f32_dpp v200, v200, v200 row_mirror row_mask:0xf bank_mask:0xf
	v_add_f32_dpp v202, v202, v202 row_mirror row_mask:0xf bank_mask:0xf
	v_add_f32_dpp v204, v204, v204 row_mirror row_mask:0xf bank_mask:0xf
	v_add_f32_dpp v206, v206, v206 row_mirror row_mask:0xf bank_mask:0xf
	v_add_f32_dpp v200, v200, v200 row_bcast:15 row_mask:0xa bank_mask:0xf
	v_add_f32_dpp v202, v202, v202 row_bcast:15 row_mask:0xa bank_mask:0xf
	v_add_f32_dpp v204, v204, v204 row_bcast:15 row_mask:0xa bank_mask:0xf
	v_add_f32_dpp v206, v206, v206 row_bcast:15 row_mask:0xa bank_mask:0xf
	s_mov_b32 exec_lo, 0xffff0000
	s_mov_b32 exec_hi, 0xffff0000
	ds_write_b32 v208, v200
	ds_write_b32 v208, v202 offset:32
	ds_write_b32 v208, v204 offset:64
	ds_write_b32 v208, v206 offset:96
	s_mov_b64 exec, -1
	v_cmp_lt_i32_e32 vcc, v121, v60
	s_nop 0
	v_mov_b32_e32 v15, v59
	v_cndmask_b32_e64 v12, 32, 0, vcc
	v_add_u32_e32 v16, v12, v121
	v_or_b32_e32 v12, v16, v101
	v_lshlrev_b32_e32 v58, 1, v12
	v_lshrrev_b32_e32 v12, 5, v0
	v_and_b32_e32 v12, 2, v12
	v_bitop3_b32 v14, v102, v100, v12 bitop3:0x36
	v_lshl_add_u64 v[12:13], v[10:11], 0, v[58:59]
	v_lshlrev_b64 v[12:13], 9, v[12:13]
	v_lshlrev_b32_e32 v16, 8, v16
	v_lshl_add_u64 v[12:13], s[4:5], 0, v[12:13]
	v_lshlrev_b32_e32 v14, 4, v14
	v_readfirstlane_b32 s6, v16
	v_add_u32_e32 v17, 0xc000, v16
	v_lshl_add_u64 v[12:13], v[12:13], 0, v[14:15]
	s_mov_b32 m0, s6
	s_mov_b64 s[6:7], 0x100
	v_readfirstlane_b32 s12, v17
	global_load_lds_dwordx4 v[12:13], off
	v_lshl_add_u64 v[12:13], v[12:13], 0, s[6:7]
	s_mov_b32 m0, s12
	v_or_b32_e32 v58, 1, v58
	global_load_lds_dwordx4 v[12:13], off
	v_lshl_add_u64 v[12:13], v[10:11], 0, v[58:59]
	v_lshlrev_b64 v[12:13], 9, v[12:13]
	v_lshl_add_u64 v[12:13], s[4:5], 0, v[12:13]
	v_lshl_add_u64 v[12:13], v[12:13], 0, v[14:15]
	v_add_u32_e32 v14, 0x6000, v16
	v_bfe_u32 v61, v0, 2, 2
	v_readfirstlane_b32 s12, v14
	v_add_u32_e32 v14, 0x12000, v16
	s_mov_b32 m0, s12
	v_readfirstlane_b32 s12, v14
	global_load_lds_dwordx4 v[12:13], off
	v_lshl_add_u64 v[12:13], v[12:13], 0, s[6:7]
	s_mov_b32 m0, s12
	v_add_u32_e32 v18, 0x23800, v117
	global_load_lds_dwordx4 v[12:13], off
	v_or_b32_e32 v12, 4, v121
	v_cmp_lt_i32_e32 vcc, v12, v60
	s_nop 1
	v_cndmask_b32_e64 v13, 32, 0, vcc
	v_add_u32_e32 v16, v13, v12
	v_or_b32_e32 v13, v16, v101
	v_lshlrev_b32_e32 v58, 1, v13
	v_bfe_u32 v12, v12, 2, 2
	v_bitop3_b32 v14, v102, v100, v12 bitop3:0x36
	v_lshl_add_u64 v[12:13], v[10:11], 0, v[58:59]
	v_lshlrev_b64 v[12:13], 9, v[12:13]
	v_lshlrev_b32_e32 v16, 8, v16
	v_lshl_add_u64 v[12:13], s[4:5], 0, v[12:13]
	v_lshlrev_b32_e32 v14, 4, v14
	v_readfirstlane_b32 s12, v16
	v_add_u32_e32 v17, 0xc000, v16
	v_lshl_add_u64 v[12:13], v[12:13], 0, v[14:15]
	s_mov_b32 m0, s12
	v_readfirstlane_b32 s12, v17
	v_or_b32_e32 v58, 1, v58
	global_load_lds_dwordx4 v[12:13], off
	v_lshl_add_u64 v[12:13], v[12:13], 0, s[6:7]
	s_mov_b32 m0, s12
	v_lshl_add_u64 v[10:11], v[10:11], 0, v[58:59]
	global_load_lds_dwordx4 v[12:13], off
	v_lshlrev_b64 v[10:11], 9, v[10:11]
	v_add_u32_e32 v12, 0x6000, v16
	v_lshl_add_u64 v[10:11], s[4:5], 0, v[10:11]
	v_readfirstlane_b32 s4, v12
	v_add_u32_e32 v12, 0x12000, v16
	v_lshl_add_u64 v[10:11], v[10:11], 0, v[14:15]
	s_mov_b32 m0, s4
	v_readfirstlane_b32 s4, v12
	global_load_lds_dwordx4 v[10:11], off
	v_lshl_add_u64 v[10:11], v[10:11], 0, s[6:7]
	s_mov_b32 m0, s4
	s_nop 0
	global_load_lds_dwordx4 v[10:11], off
	s_waitcnt lgkmcnt(0)
	s_barrier
	v_lshlrev_b32_e32 v10, 2, v0
	v_and_b32_e32 v94, 12, v10
	v_or_b32_e32 v120, v94, v61
	v_bitop3_b32 v10, v124, v94, v61 bitop3:0x1e
	v_lshl_or_b32 v14, v10, 4, v18
	v_bitop3_b32 v10, v124, v120, 1 bitop3:0x36
	v_lshl_or_b32 v19, v10, 4, v18
	s_load_dwordx4 s[4:7], s[0:1], 0x20
	s_load_dwordx2 s[12:13], s[0:1], 0x38
	ds_read_b128 v[10:13], v14
	ds_read_b128 v[62:65], v14 offset:8192
	ds_read_b128 v[14:17], v19
	ds_read_b128 v[66:69], v19 offset:8192
	v_bitop3_b32 v19, v124, v120, 4 bitop3:0x36
	v_lshl_or_b32 v19, v19, 4, v18
	v_bitop3_b32 v20, v124, v120, 5 bitop3:0x36
	v_lshl_or_b32 v20, v20, 4, v18
	ds_read_b128 v[70:73], v19
	ds_read_b128 v[78:81], v19 offset:8192
	ds_read_b128 v[74:77], v20
	ds_read_b128 v[82:85], v20 offset:8192
	v_bitop3_b32 v19, v124, v120, 8 bitop3:0x36
	v_lshl_or_b32 v19, v19, 4, v18
	v_bitop3_b32 v20, v124, v120, 9 bitop3:0x36
	v_lshl_or_b32 v20, v20, 4, v18
	ds_read_b128 v[86:89], v19
	ds_read_b128 v[104:107], v19 offset:8192
	ds_read_b128 v[90:93], v20
	ds_read_b128 v[108:111], v20 offset:8192
	v_bitop3_b32 v19, v124, v120, 12 bitop3:0x36
	v_lshl_or_b32 v19, v19, 4, v18
	v_bitop3_b32 v20, v124, v120, 13 bitop3:0x36
	v_lshl_or_b32 v18, v20, 4, v18
	ds_read_b128 v[126:129], v19
	ds_read_b128 v[134:137], v19 offset:8192
	ds_read_b128 v[130:133], v18
	ds_read_b128 v[138:141], v18 offset:8192
	v_mov_b32_e32 v103, 0x7f
	v_lshlrev_b32_e32 v58, 7, v99
	v_or_b32_e32 v122, 0x18000, v117
	s_waitcnt vmcnt(8) lgkmcnt(0)
	v_mfma_scale_f32_32x32x64_f8f6f4 v[18:33], v[2:9], v[10:17], 0, v103, v103 op_sel_hi:[0,0,0]
	v_lshlrev_b32_e32 v125, 3, v119
	v_or_b32_e32 v123, 0x1a000, v117
	v_mfma_scale_f32_32x32x64_f8f6f4 v[2:17], v[2:9], v[62:69], 0, v103, v103 op_sel_hi:[0,0,0]
	v_and_b32_e32 v62, 12, v95
	v_mfma_scale_f32_32x32x64_f8f6f4 v[18:33], v[50:57], v[70:77], v[18:33], v103, v103 op_sel_hi:[0,0,0]
	v_mfma_scale_f32_32x32x64_f8f6f4 v[2:17], v[50:57], v[78:85], v[2:17], v103, v103 op_sel_hi:[0,0,0]
	v_lshl_add_u64 v[50:51], s[10:11], 0, v[58:59]
	v_lshlrev_b32_e32 v58, 4, v119
	v_lshl_add_u64 v[54:55], v[50:51], 0, v[58:59]
	global_load_dwordx4 v[50:53], v[54:55], off
	s_brev_b32 s10, 60
	v_lshlrev_b32_e32 v58, 6, v0
	v_and_b32_e32 v58, 0x4000, v58
	v_or3_b32 v63, v122, v58, v125
	v_or3_b32 v58, v123, v58, v125
	v_mfma_scale_f32_32x32x64_f8f6f4 v[18:33], v[42:49], v[86:93], v[18:33], v103, v103 op_sel_hi:[0,0,0]
	v_mfma_scale_f32_32x32x64_f8f6f4 v[2:17], v[42:49], v[104:111], v[2:17], v103, v103 op_sel_hi:[0,0,0]
	global_load_dwordx4 v[42:45], v[54:55], off offset:32
	global_load_dwordx4 v[46:49], v[54:55], off offset:64
	s_nop 0
	global_load_dwordx4 v[54:57], v[54:55], off offset:96
	v_mfma_scale_f32_32x32x64_f8f6f4 v[2:17], v[34:41], v[134:141], v[2:17], v103, v103 op_sel_hi:[0,0,0]
	v_mfma_scale_f32_32x32x64_f8f6f4 v[18:33], v[34:41], v[126:133], v[18:33], v103, v103 op_sel_hi:[0,0,0]
	s_waitcnt vmcnt(0)
	s_nop 15
	s_nop 1
	v_fma_f32 v2, v2, s10, v50
	v_fma_f32 v3, v3, s10, v51
	v_fma_f32 v4, v4, s10, v52
	v_fma_f32 v5, v5, s10, v53
	v_cvt_pk_f16_f32 v2, v2, v3
	v_cvt_pk_f16_f32 v3, v4, v5
	v_bitop3_b32 v4, v95, v120, 12 bitop3:0x6c
	v_pk_fma_f32 v[18:19], v[18:19], s[10:11], v[50:51] op_sel_hi:[1,0,1]
	v_pk_fma_f32 v[20:21], v[20:21], s[10:11], v[52:53] op_sel_hi:[1,0,1]
	v_lshlrev_b32_e32 v4, 4, v4
	v_cvt_pk_f16_f32 v18, v18, v19
	v_cvt_pk_f16_f32 v19, v20, v21
	v_or_b32_e32 v5, v63, v4
	v_or_b32_e32 v4, v58, v4
	ds_write_b64 v5, v[18:19]
	ds_write_b64 v4, v[2:3]
	v_pk_fma_f32 v[2:3], v[22:23], s[10:11], v[42:43] op_sel_hi:[1,0,1]
	v_pk_fma_f32 v[4:5], v[6:7], s[10:11], v[42:43] op_sel_hi:[1,0,1]
	v_pk_fma_f32 v[6:7], v[24:25], s[10:11], v[44:45] op_sel_hi:[1,0,1]
	v_cvt_pk_f16_f32 v2, v2, v3
	v_cvt_pk_f16_f32 v3, v6, v7
	v_pk_fma_f32 v[6:7], v[8:9], s[10:11], v[44:45] op_sel_hi:[1,0,1]
	v_cvt_pk_f16_f32 v4, v4, v5
	v_cvt_pk_f16_f32 v5, v6, v7
	v_bitop3_b32 v6, v62, v120, 1 bitop3:0x36
	v_lshlrev_b32_e32 v6, 4, v6
	v_or_b32_e32 v7, v63, v6
	ds_write_b64 v7, v[2:3]
	v_or_b32_e32 v2, v58, v6
	ds_write_b64 v2, v[4:5]
	v_pk_fma_f32 v[2:3], v[26:27], s[10:11], v[46:47] op_sel_hi:[1,0,1]
	v_pk_fma_f32 v[6:7], v[28:29], s[10:11], v[48:49] op_sel_hi:[1,0,1]
	v_cvt_pk_f16_f32 v2, v2, v3
	v_pk_fma_f32 v[4:5], v[10:11], s[10:11], v[46:47] op_sel_hi:[1,0,1]
	v_cvt_pk_f16_f32 v3, v6, v7
	v_pk_fma_f32 v[6:7], v[12:13], s[10:11], v[48:49] op_sel_hi:[1,0,1]
	v_cvt_pk_f16_f32 v4, v4, v5
	v_cvt_pk_f16_f32 v5, v6, v7
	v_bitop3_b32 v6, v62, v120, 2 bitop3:0x36
	v_lshlrev_b32_e32 v6, 4, v6
	v_or_b32_e32 v7, v63, v6
	ds_write_b64 v7, v[2:3]
	v_or_b32_e32 v2, v58, v6
	ds_write_b64 v2, v[4:5]
	v_pk_fma_f32 v[2:3], v[30:31], s[10:11], v[54:55] op_sel_hi:[1,0,1]
	v_pk_fma_f32 v[6:7], v[32:33], s[10:11], v[56:57] op_sel_hi:[1,0,1]
	v_cvt_pk_f16_f32 v2, v2, v3
	v_pk_fma_f32 v[4:5], v[14:15], s[10:11], v[54:55] op_sel_hi:[1,0,1]
	v_cvt_pk_f16_f32 v3, v6, v7
	v_pk_fma_f32 v[6:7], v[16:17], s[10:11], v[56:57] op_sel_hi:[1,0,1]
	v_cvt_pk_f16_f32 v4, v4, v5
	v_cvt_pk_f16_f32 v5, v6, v7
	v_bitop3_b32 v6, v62, v120, 3 bitop3:0x36
	v_lshlrev_b32_e32 v6, 4, v6
	v_or_b32_e32 v7, v63, v6
	ds_write_b64 v7, v[2:3]
	v_or_b32_e32 v2, v58, v6
	ds_write_b64 v2, v[4:5]
	s_waitcnt lgkmcnt(0)
	s_barrier
	v_and_b32_e32 v236, 1, v101
	v_lshrrev_b32_e32 v237, 1, v101
	v_xor_b32_e32 v237, v237, v236
	v_lshl_or_b32 v236, v236, 1, v237
	v_lshrrev_b32_e32 v27, 8, v0
	v_lshrrev_b32_e32 v3, 3, v0
	v_and_b32_e32 v3, 16, v3
	v_mul_u32_u24_e32 v28, 0x60, v27
	v_lshlrev_b32_e32 v26, 5, v27
	v_or_b32_e32 v146, v3, v100
	v_or_b32_e32 v147, v28, v100
	v_or_b32_e32 v4, v146, v26
	v_lshlrev_b32_e32 v209, 2, v4
	v_add_u32_e32 v209, 0x27800, v209
	v_lshlrev_b32_e32 v4, 8, v4
	v_or_b32_e32 v5, 0x18000, v4
	v_bitop3_b32 v11, v236, v120, 12 bitop3:0x36
	v_or_b32_e32 v95, 0x1c000, v4
	v_lshlrev_b32_e32 v29, 3, v101
	v_bitop3_b32 v6, v236, v94, v61 bitop3:0x1e
	v_bitop3_b32 v8, v236, v120, 4 bitop3:0x36
	v_bitop3_b32 v10, v236, v120, 8 bitop3:0x36
	v_lshlrev_b32_e32 v94, 4, v11
	v_lshlrev_b32_e32 v6, 4, v6
	v_lshlrev_b32_e32 v8, 4, v8
	v_lshlrev_b32_e32 v58, 4, v10
	v_or_b32_e32 v7, v5, v6
	v_or_b32_e32 v9, v5, v8
	v_or_b32_e32 v10, v5, v58
	v_or_b32_e32 v5, v5, v94
	v_or_b32_e32 v6, v95, v6
	v_or_b32_e32 v60, v95, v8
	ds_read_b128 v[22:25], v7
	ds_read_b128 v[18:21], v9
	ds_read_b128 v[14:17], v10
	ds_read_b128 v[10:13], v5
	ds_read_b128 v[6:9], v6
	ds_read_b128 v[2:5], v60
	v_bfe_u32 v103, v0, 6, 1
	s_movk_i32 s5, 0x2000
	v_mad_u32_u24 v44, v103, 48, v147
	v_lshlrev_b32_e32 v60, 8, v44
	v_lshlrev_b32_e32 v44, 2, v44
	v_or_b32_e32 v35, v95, v58
	v_lshlrev_b32_e32 v58, 14, v99
	v_and_b32_e32 v44, 12, v44
	v_or_b32_e32 v56, v44, v61
	v_bitop3_b32 v44, v236, v44, v61 bitop3:0x1e
	v_lshl_add_u64 v[32:33], s[8:9], 0, v[58:59]
	v_lshlrev_b32_e32 v58, 4, v98
	v_or_b32_e32 v36, v95, v94
	v_lshl_add_u64 v[88:89], v[32:33], 0, v[58:59]
	v_lshl_or_b32 v57, v44, 4, v60
	ds_read_b128 v[40:43], v35
	ds_read_b128 v[106:109], v36
	s_load_dword s4, s[6:7], 0x0
	global_load_dwordx4 v[36:39], v[88:89], off
	global_load_dwordx4 v[32:35], v[88:89], off offset:1024
	ds_read_b128 v[44:47], v57
	v_bitop3_b32 v48, v236, v56, 4 bitop3:0x36
	v_lshl_or_b32 v62, v48, 4, v60
	ds_read_b128 v[48:51], v62
	v_bitop3_b32 v52, v236, v56, 8 bitop3:0x36
	v_lshl_or_b32 v63, v52, 4, v60
	ds_read_b128 v[52:55], v63
	s_waitcnt lgkmcnt(0)
	v_mfma_f32_16x16x32_f16 v[44:47], v[44:47], v[22:25], 0
	v_bitop3_b32 v64, v236, v56, 12 bitop3:0x36
	ds_read_b128 v[56:59], v57 offset:49152
	v_lshl_or_b32 v60, v64, 4, v60
	v_mfma_f32_16x16x32_f16 v[44:47], v[48:51], v[18:21], v[44:47]
	ds_read_b128 v[68:71], v60
	ds_read_b128 v[72:75], v62 offset:49152
	v_mad_u32_u24 v104, v103, 3, 1
	v_lshlrev_b32_e32 v132, 4, v104
	v_mfma_f32_16x16x32_f16 v[44:47], v[52:55], v[14:17], v[44:47]
	v_add_u32_e32 v52, v132, v147
	global_load_dwordx4 v[64:67], v[88:89], off offset:2048
	global_load_dwordx4 v[48:51], v[88:89], off offset:3072
	ds_read_b128 v[76:79], v63 offset:49152
	ds_read_b128 v[80:83], v60 offset:49152
	s_waitcnt lgkmcnt(3)
	v_mfma_f32_16x16x32_f16 v[44:47], v[68:71], v[10:13], v[44:47]
	v_lshlrev_b32_e32 v60, 8, v52
	v_lshlrev_b32_e32 v52, 2, v52
	v_and_b32_e32 v52, 12, v52
	v_mfma_f32_16x16x32_f16 v[44:47], v[56:59], v[6:9], v[44:47]
	v_or_b32_e32 v62, v52, v61
	v_bitop3_b32 v52, v236, v52, v61 bitop3:0x1e
	v_lshl_or_b32 v63, v52, 4, v60
	s_waitcnt lgkmcnt(2)
	v_mfma_f32_16x16x32_f16 v[44:47], v[72:75], v[2:5], v[44:47]
	ds_read_b128 v[52:55], v63
	v_bitop3_b32 v56, v236, v62, 4 bitop3:0x36
	v_lshl_or_b32 v84, v56, 4, v60
	s_waitcnt lgkmcnt(2)
	v_mfma_f32_16x16x32_f16 v[44:47], v[76:79], v[40:43], v[44:47]
	ds_read_b128 v[56:59], v84
	v_bitop3_b32 v68, v236, v62, 8 bitop3:0x36
	v_lshl_or_b32 v85, v68, 4, v60
	s_waitcnt lgkmcnt(2)
	v_mfma_f32_16x16x32_f16 v[110:113], v[80:83], v[106:109], v[44:47]
	ds_read_b128 v[68:71], v63 offset:49152
	v_bitop3_b32 v62, v236, v62, 12 bitop3:0x36
	v_lshl_or_b32 v60, v62, 4, v60
	ds_read_b128 v[44:47], v85
	s_waitcnt lgkmcnt(3)
	v_mfma_f32_16x16x32_f16 v[52:55], v[52:55], v[22:25], 0
	ds_read_b128 v[72:75], v60
	ds_read_b128 v[76:79], v84 offset:49152
	v_mad_u32_u24 v105, v103, 3, 2
	v_lshlrev_b32_e32 v133, 4, v105
	s_waitcnt lgkmcnt(4)
	v_mfma_f32_16x16x32_f16 v[52:55], v[56:59], v[18:21], v[52:55]
	ds_read_b128 v[56:59], v85 offset:49152
	v_add_co_u32_e32 v114, vcc, s15, v88
	s_waitcnt lgkmcnt(3)
	v_mfma_f32_16x16x32_f16 v[44:47], v[44:47], v[14:17], v[52:55]
	v_addc_co_u32_e32 v115, vcc, 0, v89, vcc
	s_waitcnt lgkmcnt(2)
	v_mfma_f32_16x16x32_f16 v[44:47], v[72:75], v[10:13], v[44:47]
	ds_read_b128 v[52:55], v60 offset:49152
	v_add_u32_e32 v60, v133, v147
	v_lshlrev_b32_e32 v72, 8, v60
	v_lshlrev_b32_e32 v60, 2, v60
	v_mfma_f32_16x16x32_f16 v[44:47], v[68:71], v[6:9], v[44:47]
	v_and_b32_e32 v60, 12, v60
	v_or_b32_e32 v68, v60, v61
	v_bitop3_b32 v60, v236, v60, v61 bitop3:0x1e
	v_lshl_or_b32 v69, v60, 4, v72
	s_waitcnt lgkmcnt(2)
	v_mfma_f32_16x16x32_f16 v[44:47], v[76:79], v[2:5], v[44:47]
	ds_read_b128 v[60:63], v69
	v_bitop3_b32 v70, v236, v68, 4 bitop3:0x36
	v_lshl_or_b32 v70, v70, 4, v72
	s_waitcnt lgkmcnt(2)
	v_mfma_f32_16x16x32_f16 v[44:47], v[56:59], v[40:43], v[44:47]
	ds_read_b128 v[56:59], v70
	v_bitop3_b32 v71, v236, v68, 8 bitop3:0x36
	v_lshl_or_b32 v71, v71, 4, v72
	s_waitcnt lgkmcnt(1)
	v_mfma_f32_16x16x32_f16 v[22:25], v[60:63], v[22:25], 0
	v_bitop3_b32 v60, v236, v68, 12 bitop3:0x36
	v_lshl_or_b32 v68, v60, 4, v72
	ds_read_b32 v210, v209
	v_mfma_f32_16x16x32_f16 v[126:129], v[52:55], v[106:109], v[44:47]
	s_nop 2
	ds_read_b128 v[44:47], v71
	ds_read_b128 v[52:55], v69 offset:49152
	ds_read_b128 v[60:63], v70 offset:49152
	s_waitcnt lgkmcnt(4)
	v_mfma_f32_16x16x32_f16 v[18:21], v[56:59], v[18:21], v[22:25]
	ds_read_b128 v[56:59], v71 offset:49152
	s_nop 1
	ds_read_b128 v[22:25], v68
	s_waitcnt lgkmcnt(4)
	v_mfma_f32_16x16x32_f16 v[14:17], v[44:47], v[14:17], v[18:21]
	v_add_co_u32_e32 v44, vcc, s5, v88
	s_movk_i32 s5, 0x3000
	s_nop 0
	ds_read_b128 v[18:21], v68 offset:49152
	s_waitcnt lgkmcnt(1)
	v_mfma_f32_16x16x32_f16 v[10:13], v[22:25], v[10:13], v[14:17]
	v_addc_co_u32_e32 v45, vcc, 0, v89, vcc
	global_load_dwordx4 v[84:87], v[114:115], off offset:1024
	global_load_dwordx4 v[80:83], v[114:115], off offset:2048
	global_load_dwordx4 v[92:95], v[44:45], off offset:-4096
	global_load_dwordx4 v[76:79], v[44:45], off
	v_mfma_f32_16x16x32_f16 v[6:9], v[52:55], v[6:9], v[10:13]
	global_load_dwordx4 v[72:75], v[44:45], off offset:1024
	global_load_dwordx4 v[68:71], v[44:45], off offset:2048
	global_load_dwordx4 v[52:55], v[44:45], off offset:3072
	v_mov_b32_e32 v13, 0xff61b1e6
	v_mfma_f32_16x16x32_f16 v[2:5], v[60:63], v[2:5], v[6:9]
	s_nop 2
	v_add_co_u32_e32 v6, vcc, s5, v88
	v_mfma_f32_16x16x32_f16 v[2:5], v[56:59], v[40:43], v[2:5]
	s_nop 0
	v_addc_co_u32_e32 v7, vcc, 0, v89, vcc
	global_load_dwordx4 v[88:91], v[114:115], off offset:3072
	global_load_dwordx4 v[60:63], v[6:7], off
	global_load_dwordx4 v[56:59], v[6:7], off offset:1024
	global_load_dwordx4 v[44:47], v[6:7], off offset:2048
	global_load_dwordx4 v[40:43], v[6:7], off offset:3072
	s_waitcnt lgkmcnt(0)
	v_mfma_f32_16x16x32_f16 v[16:19], v[18:21], v[106:109], v[2:5]
	s_mov_b32 s5, 0xff61b1e6
	s_nop 0
	v_or_b32_e32 v3, s14, v146
	v_mov_b32_e32 v4, 0x7df
	v_med3_u32 v3, v3, 32, v4
	v_or_b32_e32 v4, v97, v102
	v_sub_u32_e32 v3, v4, v3
	v_add_f32_e32 v2, s4, v210
	v_add_u32_e32 v3, 32, v3
	v_mad_u32_u24 v4, v103, 48, v3
	s_movk_i32 s4, 0x41
	v_add_f32_e32 v5, v2, v110
	v_mul_f32_e32 v5, 0x3db8aa3b, v5
	v_cmp_gt_u32_e32 vcc, s4, v4
	v_add_u32_e32 v6, 1, v4
	v_add_f32_e32 v7, v2, v111
	v_cndmask_b32_e32 v5, v13, v5, vcc
	v_mul_f32_e32 v7, 0x3db8aa3b, v7
	v_cmp_gt_u32_e32 vcc, s4, v6
	v_add_u32_e32 v8, 2, v4
	v_add_f32_e32 v9, v2, v112
	v_cndmask_b32_e32 v6, v13, v7, vcc
	v_mul_f32_e32 v9, 0x3db8aa3b, v9
	v_cmp_gt_u32_e32 vcc, s4, v8
	v_add_u32_e32 v4, 3, v4
	v_max3_f32 v7, v5, s5, v6
	v_cndmask_b32_e32 v8, v13, v9, vcc
	v_add_f32_e32 v9, v2, v113
	v_mul_f32_e32 v9, 0x3db8aa3b, v9
	v_cmp_gt_u32_e32 vcc, s4, v4
	v_add_u32_e32 v11, v3, v132
	v_add_f32_e32 v12, v2, v127
	v_cndmask_b32_e32 v10, v13, v9, vcc
	v_max3_f32 v4, v7, v8, v10
	v_add_f32_e32 v7, v2, v126
	v_mul_f32_e32 v7, 0x3db8aa3b, v7
	v_cmp_gt_u32_e32 vcc, s4, v11
	v_add_u32_e32 v9, 1, v11
	v_mul_f32_e32 v12, 0x3db8aa3b, v12
	v_cndmask_b32_e32 v7, v13, v7, vcc
	v_cmp_gt_u32_e32 vcc, s4, v9
	v_add_f32_e32 v14, v2, v128
	v_mul_f32_e32 v14, 0x3db8aa3b, v14
	v_cndmask_b32_e32 v9, v13, v12, vcc
	v_add_u32_e32 v12, 2, v11
	v_cmp_gt_u32_e32 vcc, s4, v12
	v_add_u32_e32 v11, 3, v11
	v_add_u32_e32 v3, v3, v133
	v_cndmask_b32_e32 v12, v13, v14, vcc
	v_add_f32_e32 v14, v2, v129
	v_mul_f32_e32 v14, 0x3db8aa3b, v14
	v_cmp_gt_u32_e32 vcc, s4, v11
	v_add_f32_e32 v11, v2, v16
	v_mul_f32_e32 v11, 0x3db8aa3b, v11
	v_cndmask_b32_e32 v15, v13, v14, vcc
	v_cmp_gt_u32_e32 vcc, s4, v3
	v_add_u32_e32 v14, 1, v3
	v_add_f32_e32 v16, v2, v17
	v_cndmask_b32_e32 v11, v13, v11, vcc
	v_mul_f32_e32 v16, 0x3db8aa3b, v16
	v_cmp_gt_u32_e32 vcc, s4, v14
	v_add_f32_e32 v17, v2, v18
	v_max3_f32 v4, v4, v7, v9
	v_cndmask_b32_e32 v14, v13, v16, vcc
	v_add_u32_e32 v16, 2, v3
	v_mul_f32_e32 v17, 0x3db8aa3b, v17
	v_cmp_gt_u32_e32 vcc, s4, v16
	v_add_u32_e32 v3, 3, v3
	v_add_f32_e32 v2, v2, v19
	v_max3_f32 v4, v4, v12, v15
	v_cndmask_b32_e32 v16, v13, v17, vcc
	v_mul_f32_e32 v2, 0x3db8aa3b, v2
	v_cmp_gt_u32_e32 vcc, s4, v3
	v_max3_f32 v4, v4, v11, v14
	v_lshlrev_b32_e32 v126, 5, v99
	v_cndmask_b32_e32 v17, v13, v2, vcc
	v_max3_f32 v2, v4, v16, v17
	v_mov_b32_e32 v3, v2
	v_lshlrev_b32_e32 v127, 2, v119
	v_lshrrev_b32_e32 v4, 7, v0
	v_cmp_gt_u32_e32 vcc, 16, v98
	v_permlane16_swap_b32_e32 v3, v2
	v_max_f32_e32 v2, v2, v3
	v_mov_b32_e32 v3, v2
	s_nop 1
	v_permlane32_swap_b32_e32 v3, v2
	v_max_f32_e32 v13, v2, v3
	v_and_b32_e32 v2, 0x180, v0
	v_or_b32_e32 v2, 0x23400, v2
	v_lshlrev_b32_e32 v3, 2, v100
	s_and_saveexec_b64 s[4:5], vcc
	v_lshlrev_b32_e32 v18, 6, v103
	v_add3_u32 v18, v2, v18, v3
	ds_write_b32 v18, v13
	s_or_b64 exec, exec, s[4:5]
	v_lshlrev_b32_e32 v18, 4, v103
	v_bitop3_b32 v19, v18, 16, v100 bitop3:0x36
	v_lshl_add_u32 v2, v19, 2, v2
	s_waitcnt lgkmcnt(0)
	s_barrier
	ds_read_b32 v19, v2
	v_max_f32_e32 v13, v13, v13
	v_mul_u32_u24_e32 v20, 0xd00, v4
	s_load_dwordx2 s[0:1], s[0:1], 0x30
	v_or_b32_e32 v2, 1, v124
	s_waitcnt lgkmcnt(0)
	v_max_f32_e32 v19, v19, v19
	v_max_f32_e32 v19, v13, v19
	v_sub_f32_e32 v5, v5, v19
	v_exp_f32_e32 v5, v5
	v_sub_f32_e32 v6, v6, v19
	v_exp_f32_e32 v6, v6
	v_sub_f32_e32 v8, v8, v19
	v_mul_u32_u24_e32 v13, 0xd0, v100
	v_exp_f32_e32 v8, v8
	v_sub_f32_e32 v10, v10, v19
	v_add3_u32 v20, v13, v20, v29
	v_exp_f32_e32 v10, v10
	v_or_b32_e32 v22, 0x20000, v20
	v_add_f32_e32 v20, 0, v5
	v_add_f32_e32 v20, v20, v6
	v_add_f32_e32 v20, v20, v8
	v_add_f32_e32 v23, v20, v10
	v_cvt_pk_f16_f32 v21, v8, v10
	v_cvt_pk_f16_f32 v20, v5, v6
	v_mad_u32_u24 v5, v103, s16, v22
	ds_write_b64 v5, v[20:21]
	v_sub_f32_e32 v5, v7, v19
	v_exp_f32_e32 v5, v5
	v_sub_f32_e32 v6, v9, v19
	v_exp_f32_e32 v6, v6
	v_sub_f32_e32 v7, v12, v19
	v_exp_f32_e32 v7, v7
	v_sub_f32_e32 v8, v15, v19
	v_exp_f32_e32 v8, v8
	v_sub_f32_e32 v10, v11, v19
	v_add_f32_e32 v9, v23, v5
	v_exp_f32_e32 v10, v10
	v_sub_f32_e32 v11, v14, v19
	v_add_f32_e32 v9, v9, v6
	v_exp_f32_e32 v11, v11
	v_sub_f32_e32 v12, v16, v19
	v_add_f32_e32 v9, v9, v7
	v_exp_f32_e32 v12, v12
	v_sub_f32_e32 v14, v17, v19
	v_add_f32_e32 v9, v9, v8
	v_exp_f32_e32 v14, v14
	v_add_f32_e32 v9, v9, v10
	v_add_f32_e32 v9, v9, v11
	v_add_f32_e32 v9, v9, v12
	v_add_f32_e32 v9, v9, v14
	v_mov_b32_e32 v15, v9
	v_cvt_pk_f16_f32 v7, v7, v8
	v_cvt_pk_f16_f32 v6, v5, v6
	v_lshl_add_u32 v5, v104, 5, v22
	ds_write_b64 v5, v[6:7]
	v_permlane16_swap_b32_e32 v15, v9
	v_add_f32_e32 v5, v9, v15
	v_mov_b32_e32 v6, v5
	s_movk_i32 s7, 0xd00
	s_mov_b32 s6, 0x20000
	v_cvt_pk_f16_f32 v9, v12, v14
	v_cvt_pk_f16_f32 v8, v10, v11
	v_lshl_add_u32 v7, v105, 5, v22
	ds_write_b64 v7, v[8:9]
	v_permlane32_swap_b32_e32 v6, v5
	s_and_saveexec_b64 s[4:5], vcc
	s_cbranch_execz .LBB1_4
	v_lshlrev_b32_e32 v4, 5, v4
	v_or_b32_e32 v7, v18, v100
	v_lshlrev_b32_e32 v4, 2, v4
	v_lshlrev_b32_e32 v7, 2, v7
	s_mov_b32 s8, 0x23600
	v_add3_u32 v4, v7, v4, s8
	v_add_f32_e32 v5, v5, v6
	ds_write_b32 v4, v5

	.amdhsa_kernel _Z7na_mainPKDF16_PKhS0_PKfS4_S4_S4_Pf
		.amdhsa_group_segment_fixed_size 162048
		.amdhsa_private_segment_fixed_size 0
		.amdhsa_kernarg_size 64
		.amdhsa_user_sgpr_count 2
		.amdhsa_user_sgpr_dispatch_ptr 0
		.amdhsa_user_sgpr_queue_ptr 0
		.amdhsa_user_sgpr_kernarg_segment_ptr 1
		.amdhsa_user_sgpr_dispatch_id 0
		.amdhsa_user_sgpr_kernarg_preload_length 0
		.amdhsa_user_sgpr_kernarg_preload_offset 0
		.amdhsa_user_sgpr_private_segment_size 0
		.amdhsa_uses_dynamic_stack 0
		.amdhsa_enable_private_segment 0
		.amdhsa_system_sgpr_workgroup_id_x 1
		.amdhsa_system_sgpr_workgroup_id_y 0
		.amdhsa_system_sgpr_workgroup_id_z 0
		.amdhsa_system_sgpr_workgroup_info 0
		.amdhsa_system_vgpr_workitem_id 0
		.amdhsa_next_free_vgpr 238
		.amdhsa_next_free_sgpr 96
		.amdhsa_accum_offset 240
		.amdhsa_reserve_vcc 1
		.amdhsa_float_round_mode_32 0
		.amdhsa_float_round_mode_16_64 0
		.amdhsa_float_denorm_mode_32 3
		.amdhsa_float_denorm_mode_16_64 3
		.amdhsa_dx10_clamp 1
		.amdhsa_ieee_mode 1
		.amdhsa_fp16_overflow 0
		.amdhsa_tg_split 0
		.amdhsa_exception_fp_ieee_invalid_op 0
		.amdhsa_exception_fp_denorm_src 0
		.amdhsa_exception_fp_ieee_div_zero 0
		.amdhsa_exception_fp_ieee_overflow 0
		.amdhsa_exception_fp_ieee_underflow 0
		.amdhsa_exception_fp_ieee_inexact 0
		.amdhsa_exception_int_div_zero 0
	.end_amdhsa_kernel

amdhsa.kernels:
  - .agpr_count:     16
    .args:
      - .actual_access:  read_only
        .address_space:  global
        .offset:         0
        .size:           8
        .value_kind:     global_buffer
      - .actual_access:  read_only
        .address_space:  global
        .offset:         8
        .size:           8
        .value_kind:     global_buffer
      - .actual_access:  read_only
        .address_space:  global
        .offset:         16
        .size:           8
        .value_kind:     global_buffer
      - .actual_access:  read_only
        .address_space:  global
        .offset:         24
        .size:           8
        .value_kind:     global_buffer
      - .actual_access:  read_only
        .address_space:  global
        .offset:         32
        .size:           8
        .value_kind:     global_buffer
      - .actual_access:  read_only
        .address_space:  global
        .offset:         40
        .size:           8
        .value_kind:     global_buffer
      - .actual_access:  write_only
        .address_space:  global
        .offset:         48
        .size:           8
        .value_kind:     global_buffer
      - .actual_access:  write_only
        .address_space:  global
        .offset:         56
        .size:           8
        .value_kind:     global_buffer
      - .actual_access:  write_only
        .address_space:  global
        .offset:         64
        .size:           8
        .value_kind:     global_buffer
      - .actual_access:  write_only
        .address_space:  global
        .offset:         72
        .size:           8
        .value_kind:     global_buffer
      - .actual_access:  write_only
        .address_space:  global
        .offset:         80
        .size:           8
        .value_kind:     global_buffer
      - .actual_access:  write_only
        .address_space:  global
        .offset:         88
        .size:           8
        .value_kind:     global_buffer
    .group_segment_fixed_size: 50176
    .kernarg_segment_align: 8
    .kernarg_segment_size: 96
    .language:       OpenCL C
    .language_version:
      - 2
      - 0
    .max_flat_workgroup_size: 256
    .name:           _Z7na_prepPKfS0_S0_S0_S0_S0_PDF16_PhS1_PfS3_S3_
    .private_segment_fixed_size: 0
    .sgpr_count:     23
    .sgpr_spill_count: 0
    .symbol:         _Z7na_prepPKfS0_S0_S0_S0_S0_PDF16_PhS1_PfS3_S3_.kd
    .uniform_work_group_size: 1
    .uses_dynamic_stack: false
    .vgpr_count:     116
    .vgpr_spill_count: 0
    .wavefront_size: 64
  - .agpr_count:     0
    .args:
      - .address_space:  global
        .offset:         0
        .size:           8
        .value_kind:     global_buffer
      - .actual_access:  read_only
        .address_space:  global
        .offset:         8
        .size:           8
        .value_kind:     global_buffer
      - .actual_access:  read_only
        .address_space:  global
        .offset:         16
        .size:           8
        .value_kind:     global_buffer
      - .actual_access:  read_only
        .address_space:  global
        .offset:         24
        .size:           8
        .value_kind:     global_buffer
      - .actual_access:  read_only
        .address_space:  global
        .offset:         32
        .size:           8
        .value_kind:     global_buffer
      - .actual_access:  read_only
        .address_space:  global
        .offset:         40
        .size:           8
        .value_kind:     global_buffer
      - .actual_access:  read_only
        .address_space:  global
        .offset:         48
        .size:           8
        .value_kind:     global_buffer
      - .actual_access:  write_only
        .address_space:  global
        .offset:         56
        .size:           8
        .value_kind:     global_buffer
    .group_segment_fixed_size: 162048
    .kernarg_segment_align: 8
    .kernarg_segment_size: 64
    .language:       OpenCL C
    .language_version:
      - 2
      - 0
    .max_flat_workgroup_size: 512
    .name:           _Z7na_mainPKDF16_PKhS0_PKfS4_S4_S4_Pf
    .private_segment_fixed_size: 0
    .sgpr_count:     24
    .sgpr_spill_count: 0
    .symbol:         _Z7na_mainPKDF16_PKhS0_PKfS4_S4_S4_Pf.kd
    .uniform_work_group_size: 1
    .uses_dynamic_stack: false
    .vgpr_count:     238
    .vgpr_spill_count: 0
    .wavefront_size: 64
